# conversion tickets cover 4 tiles (two chunk pairs run back to back), ticket table shortened accordingly
# speedup vs baseline: 1.0030x; 1.0030x over previous
; __device__ __forceinline__ void attn_conv_phase(const Ptrs& P, const att::AttnArgs& A, int layer, unsigned* qctr, unsigned char* lds, const int wave_) {
;     ...
;     for (;;) {
;         __syncthreads();
;         if (t0_) TK[0] = nxt_;
;         __syncthreads();
;         const int tk = __builtin_amdgcn_readfirstlane(TK[0]);
;         if (tk >= att::N_TICKETS) break;
;         if (t0_) nxt_ = (int)__hip_atomic_fetch_add(qctr, 1u, __ATOMIC_RELAXED, __HIP_MEMORY_SCOPE_AGENT);
.Lticket_top_nowait:
	s_barrier
	s_and_saveexec_b64 s[0:1], s[88:89]
	v_mov_b32_e32 v0, s71
	ds_write_b32 v0, v133
	s_or_b64 exec, exec, s[0:1]
	v_mov_b32_e32 v0, s71
	s_waitcnt lgkmcnt(0)
	s_barrier
	ds_read_b32 v0, v0
	s_mov_b64 s[14:15], -1
	s_waitcnt lgkmcnt(0)
	v_readfirstlane_b32 s0, v0
	s_cmpk_gt_i32 s0, 0xce5
	s_cbranch_scc1 .LBB0_439
	s_and_saveexec_b64 s[14:15], s[88:89]
	s_cbranch_execz .LBB0_447
	s_mov_b64 s[22:23], exec
	v_mbcnt_lo_u32_b32 v0, s22, 0
	v_mbcnt_hi_u32_b32 v0, s23, v0
	v_cmp_eq_u32_e32 vcc, 0, v0
	s_and_saveexec_b64 s[18:19], vcc
	s_cbranch_execz .LBB0_446
	s_bcnt1_i32_b64 s1, s[22:23]
	v_mov_b32_e32 v2, s1
	global_atomic_add v133, v1, v2, s[86:87] sc0

; #define LAS __attribute__((address_space(3)))
; __device__ __forceinline__ CvTile cv_decode(const Ptrs& P, int it) {
;     constexpr int T_IN = (D / 128) * (NQKV / 256), T_O = (D / 128) * (D / 256), T_G = (D / 128) * (FF / 256), T_D = (FF / 128) * (D / 256), T_E = 2 * T_G + T_D;
;     CvTile c; int r = it; c.gain = nullptr; c.pitch = 0;
;     if (r < T_IN) { c.W = P.w_in; c.WT = (unsigned char*)P.Wqkv_t; c.K = D; c.N = NQKV; c.mode = 0; c.f8 = 0; c.r = r; return c; } r -= T_IN;
;     if (r < T_O) { c.W = P.w_out; c.WT = (unsigned char*)P.Wo_t; c.K = D; c.N = D; c.mode = 0; c.f8 = (WO8_LAYER == 0) ? 1 : 0; c.r = r; return c; } r -= T_O;
;     if (r < T_G) { c.W = P.dwg; c.WT = P.Wgu_d; c.K = D; c.N = FF; c.mode = 1; c.f8 = 1; c.r = r; return c; } r -= T_G;
;     if (r < T_G) { c.W = P.dwu; c.WT = P.Wgu_d; c.K = D; c.N = FF; c.mode = 2; c.f8 = 1; c.r = r; return c; } r -= T_G;
;     if (r < T_D) { c.W = P.dwd; c.WT = P.Wd_d; c.K = FF; c.N = D; c.mode = 0; c.f8 = 1; c.r = r; return c; } r -= T_D;
;     if (r < T_IN) { const int kb = r / 24, nb = r - kb * 24; c.K = D; c.mode = 0; c.pitch = NQKV; c.gain = P.attn_norm + D;
;         c.W = P.w_in + (size_t)D * NQKV; c.WT = P.Wv8; c.N = NQKV; c.f8 = 1; c.r = kb * 24 + nb;
;         return c; } r -= T_IN;
;     if (r < T_O) { c.W = P.w_out + (size_t)D * D; c.WT = (unsigned char*)(P.Wo_t + (size_t)D * D); c.K = D; c.N = D; c.mode = 0; c.f8 = (WO8_LAYER == 1) ? 1 : 0; c.r = r; return c; } r -= T_O;
;     const int e = r / T_E; r -= e * T_E; c.f8 = 1;
;     if (r < T_G) { c.W = P.mwg + (size_t)e * D * FF; c.WT = P.Wgu_m + (size_t)e * NGU * D; c.K = D; c.N = FF; c.mode = 1; c.r = r; return c; } r -= T_G;
;     if (r < T_G) { c.W = P.mwu + (size_t)e * D * FF; c.WT = P.Wgu_m + (size_t)e * NGU * D; c.K = D; c.N = FF; c.mode = 2; c.r = r; return c; } r -= T_G;
;     c.W = P.mwd + (size_t)e * FF * D; c.WT = P.Wd_m + (size_t)e * D * FF; c.K = FF; c.N = D; c.mode = 0; c.r = r; return c;
; __device__ __forceinline__ void attn_conv_phase(const Ptrs& P, const att::AttnArgs& A, int layer, unsigned* qctr, unsigned char* lds, const int wave_) {
;     ...
;         const int code = att::ATT_ORDER.v[tk];
;         if (code & 0x8000) {
;             const int t0 = CV_L0 + (layer * att::N_CHUNKS + (code & 0x7fff)) * att::CHUNK_TILES;
;             convert_weights(P, (LAS unsigned char*)lds, t0, 1, t0 + att::CHUNK_TILES, wave_, lane_id());
.LBB0_447:
	s_or_b64 exec, exec, s[14:15]
	s_ashr_i32 s1, s0, 31
	s_xor_b64 s[24:25], s[20:21], -1
	s_lshl_b64 s[0:1], s[0:1], 1
	s_getpc_b64 s[14:15]
	s_add_u32 s14, s14, _ZN3attL9ATT_ORDERE@rel32@lo+4
	s_addc_u32 s15, s15, _ZN3attL9ATT_ORDERE@rel32@hi+12
	s_add_u32 s0, s14, s0
	s_addc_u32 s1, s15, s1
	s_and_b32 s14, s0, 2
	s_and_b32 s0, s0, -4
	s_load_dword s26, s[0:1], 0x0
	s_lshl_b32 s14, s14, 3
	v_mov_b32_e32 v2, -1
	s_waitcnt lgkmcnt(0)
	s_lshr_b32 s26, s26, s14
	s_and_b32 s26, s26, 0xffff
	s_mov_b32 s14, s26
	v_mov_b32_e32 v0, s26
	s_bitcmp0_b32 s26, 15
	s_cselect_b64 s[0:1], -1, 0
	s_and_b64 vcc, exec, s[0:1]
	s_mov_b64 s[0:1], -1
	s_cbranch_vccnz .LBB0_500
	s_and_b32 s15, s26, 0x7fff
	s_mul_i32 s0, s80, 0x420
	s_add_i32 s15, s15, s0
	s_lshl_b32 s15, s15, 1
	s_lshl_b32 s14, s15, 1
	s_cmpk_gt_u32 s15, 0xbf
	v_mbcnt_lo_u32_b32 v132, -1, 0
	v_mbcnt_hi_u32_b32 v132, -1, v132
	s_cselect_b64 s[42:43], -1, 0
	s_cmpk_lt_u32 s15, 0xc0
	s_mov_b64 s[28:29], -1
	s_cbranch_scc1 .LBB0_460
	s_cmpk_gt_u32 s15, 0xff
	s_mov_b64 s[0:1], -1
	s_cbranch_scc0 .LBB0_458
	s_add_i32 s0, s14, 0xfffffe00
	s_mul_hi_u32 s1, s0, 0x3e0f83e1
	s_lshr_b32 s23, s1, 8
	s_mul_i32 s22, s23, 0xfffffbe0
	s_add_i32 s22, s22, s0
	s_cmpk_gt_i32 s22, 0x15f
	s_mul_hi_u32 s27, s23, 0x2c00000
	s_mul_i32 s30, s23, 0x2c00000
	s_mov_b64 s[0:1], -1
	s_cbranch_scc0 .LBB0_455
	s_mov_b64 s[72:73], -1
	s_cmpk_gt_u32 s22, 0x2bf
	s_cbranch_scc0 .LBB0_453
	s_add_i32 s18, s22, 0xfffffd40
	v_readlane_b32 s0, v254, 49
	v_readlane_b32 s1, v254, 50
	s_add_u32 s46, s0, s30
	s_addc_u32 s47, s1, s27
	s_mul_i32 s1, s23, 0xb00000
	v_readlane_b32 s2, v254, 58
	s_mul_hi_u32 s0, s23, 0xb00000
	s_add_u32 s66, s2, s1
	v_readlane_b32 s1, v254, 59
	s_addc_u32 s67, s1, s0
	s_mov_b64 s[0:1], 0

.LBB0_489:
.Lpb1_489:
	v_readlane_b32 s78, v255, 22
	s_cmp_eq_u64 s[28:29], 0
	v_readlane_b32 s68, v254, 36
	s_movk_i32 s66, 0xb00
	v_readlane_b32 s2, v254, 45
	v_readlane_b32 s79, v255, 23
	v_readlane_b32 s69, v254, 37
	s_cbranch_scc1 .Lpb1_491
	s_ashr_i32 s71, s70, 31
	s_lshl_b64 s[0:1], s[70:71], 2
	s_add_u32 s0, s28, s0
	s_addc_u32 s1, s29, s1
	s_lshl_b32 s14, s96, 2
	s_load_dwordx16 s[40:55], s[0:1], s14 offset:0x0
	s_waitcnt lgkmcnt(0)
	s_mov_b32 s0, s43
	s_waitcnt vmcnt(12)
	v_pk_mul_f32 v[16:17], v[16:17], s[0:1] op_sel_hi:[1,0]
	v_pk_mul_f32 v[14:15], v[14:15], s[0:1] op_sel_hi:[1,0]
	s_mov_b32 s0, s45
	s_waitcnt vmcnt(10)
	v_pk_mul_f32 v[24:25], v[24:25], s[0:1] op_sel_hi:[1,0]
	v_pk_mul_f32 v[22:23], v[22:23], s[0:1] op_sel_hi:[1,0]
	s_mov_b32 s0, s47
	s_waitcnt vmcnt(8)
	v_pk_mul_f32 v[32:33], v[32:33], s[0:1] op_sel_hi:[1,0]
	v_pk_mul_f32 v[30:31], v[30:31], s[0:1] op_sel_hi:[1,0]
	s_mov_b32 s0, s49
	s_waitcnt vmcnt(6)
	v_pk_mul_f32 v[40:41], v[40:41], s[0:1] op_sel_hi:[1,0]
	v_pk_mul_f32 v[38:39], v[38:39], s[0:1] op_sel_hi:[1,0]
	s_mov_b32 s0, s51
	s_waitcnt vmcnt(4)
	v_pk_mul_f32 v[48:49], v[48:49], s[0:1] op_sel_hi:[1,0]
	v_pk_mul_f32 v[46:47], v[46:47], s[0:1] op_sel_hi:[1,0]
	s_mov_b32 s0, s53
	s_waitcnt vmcnt(2)
	v_pk_mul_f32 v[56:57], v[56:57], s[0:1] op_sel_hi:[1,0]
	v_pk_mul_f32 v[54:55], v[54:55], s[0:1] op_sel_hi:[1,0]
	s_mov_b32 s0, s55
	v_pk_mul_f32 v[4:5], v[4:5], s[40:41] op_sel_hi:[1,0]
	v_pk_mul_f32 v[2:3], v[2:3], s[40:41] op_sel_hi:[1,0]
	v_pk_mul_f32 v[8:9], v[8:9], s[40:41] op_sel:[0,1]
	v_pk_mul_f32 v[6:7], v[6:7], s[40:41] op_sel:[0,1]
	v_pk_mul_f32 v[12:13], v[12:13], s[42:43] op_sel_hi:[1,0]
	v_pk_mul_f32 v[10:11], v[10:11], s[42:43] op_sel_hi:[1,0]
	v_pk_mul_f32 v[20:21], v[20:21], s[44:45] op_sel_hi:[1,0]
	v_pk_mul_f32 v[18:19], v[18:19], s[44:45] op_sel_hi:[1,0]
	v_pk_mul_f32 v[28:29], v[28:29], s[46:47] op_sel_hi:[1,0]
	v_pk_mul_f32 v[26:27], v[26:27], s[46:47] op_sel_hi:[1,0]
	v_pk_mul_f32 v[36:37], v[36:37], s[48:49] op_sel_hi:[1,0]
	v_pk_mul_f32 v[34:35], v[34:35], s[48:49] op_sel_hi:[1,0]
	v_pk_mul_f32 v[44:45], v[44:45], s[50:51] op_sel_hi:[1,0]
	v_pk_mul_f32 v[42:43], v[42:43], s[50:51] op_sel_hi:[1,0]
	v_pk_mul_f32 v[52:53], v[52:53], s[52:53] op_sel_hi:[1,0]
	v_pk_mul_f32 v[50:51], v[50:51], s[52:53] op_sel_hi:[1,0]
	s_waitcnt vmcnt(1)
	v_pk_mul_f32 v[60:61], v[60:61], s[54:55] op_sel_hi:[1,0]
	v_pk_mul_f32 v[58:59], v[58:59], s[54:55] op_sel_hi:[1,0]
	s_waitcnt vmcnt(0)
	v_pk_mul_f32 v[64:65], v[64:65], s[0:1] op_sel_hi:[1,0]
	v_pk_mul_f32 v[62:63], v[62:63], s[0:1] op_sel_hi:[1,0]

; #define LAS __attribute__((address_space(3)))
; __device__ __forceinline__ CvTile cv_decode(const Ptrs& P, int it) {
;     constexpr int T_IN = (D / 128) * (NQKV / 256), T_O = (D / 128) * (D / 256), T_G = (D / 128) * (FF / 256), T_D = (FF / 128) * (D / 256), T_E = 2 * T_G + T_D;
;     CvTile c; int r = it; c.gain = nullptr; c.pitch = 0;
;     if (r < T_IN) { c.W = P.w_in; c.WT = (unsigned char*)P.Wqkv_t; c.K = D; c.N = NQKV; c.mode = 0; c.f8 = 0; c.r = r; return c; } r -= T_IN;
;     if (r < T_O) { c.W = P.w_out; c.WT = (unsigned char*)P.Wo_t; c.K = D; c.N = D; c.mode = 0; c.f8 = (WO8_LAYER == 0) ? 1 : 0; c.r = r; return c; } r -= T_O;
;     if (r < T_G) { c.W = P.dwg; c.WT = P.Wgu_d; c.K = D; c.N = FF; c.mode = 1; c.f8 = 1; c.r = r; return c; } r -= T_G;
;     if (r < T_G) { c.W = P.dwu; c.WT = P.Wgu_d; c.K = D; c.N = FF; c.mode = 2; c.f8 = 1; c.r = r; return c; } r -= T_G;
;     if (r < T_D) { c.W = P.dwd; c.WT = P.Wd_d; c.K = FF; c.N = D; c.mode = 0; c.f8 = 1; c.r = r; return c; } r -= T_D;
;     if (r < T_IN) { const int kb = r / 24, nb = r - kb * 24; c.K = D; c.mode = 0; c.pitch = NQKV; c.gain = P.attn_norm + D;
;         c.W = P.w_in + (size_t)D * NQKV; c.WT = P.Wv8; c.N = NQKV; c.f8 = 1; c.r = kb * 24 + nb;
;         return c; } r -= T_IN;
;     if (r < T_O) { c.W = P.w_out + (size_t)D * D; c.WT = (unsigned char*)(P.Wo_t + (size_t)D * D); c.K = D; c.N = D; c.mode = 0; c.f8 = (WO8_LAYER == 1) ? 1 : 0; c.r = r; return c; } r -= T_O;
;     const int e = r / T_E; r -= e * T_E; c.f8 = 1;
;     if (r < T_G) { c.W = P.mwg + (size_t)e * D * FF; c.WT = P.Wgu_m + (size_t)e * NGU * D; c.K = D; c.N = FF; c.mode = 1; c.r = r; return c; } r -= T_G;
;     if (r < T_G) { c.W = P.mwu + (size_t)e * D * FF; c.WT = P.Wgu_m + (size_t)e * NGU * D; c.K = D; c.N = FF; c.mode = 2; c.r = r; return c; } r -= T_G;
;     c.W = P.mwd + (size_t)e * FF * D; c.WT = P.Wd_m + (size_t)e * D * FF; c.K = FF; c.N = D; c.mode = 0; c.r = r; return c;
; __device__ __forceinline__ void attn_conv_phase(const Ptrs& P, const att::AttnArgs& A, int layer, unsigned* qctr, unsigned char* lds, const int wave_) {
;     ...
;             const int t0 = CV_L0 + (layer * att::N_CHUNKS + (code & 0x7fff)) * att::CHUNK_TILES;
;             convert_weights(P, (LAS unsigned char*)lds, t0, 1, t0 + att::CHUNK_TILES, wave_, lane_id());
.Lpipe_b1_done:
	s_and_b32 s15, s26, 0x7fff
	s_mul_i32 s0, s80, 0x420
	s_add_i32 s15, s15, s0
	s_lshl_b32 s15, s15, 1
	s_add_i32 s15, s15, 1
	s_lshl_b32 s14, s15, 1
	s_cmpk_gt_u32 s15, 0xbf
	v_mbcnt_lo_u32_b32 v132, -1, 0
	v_mbcnt_hi_u32_b32 v132, -1, v132
	s_cselect_b64 s[42:43], -1, 0
	s_cmpk_lt_u32 s15, 0xc0
	s_mov_b64 s[28:29], -1
	s_cbranch_scc1 .Lpc_460
	s_cmpk_gt_u32 s15, 0xff
	s_mov_b64 s[0:1], -1
	s_cbranch_scc0 .Lpc_458
	s_add_i32 s0, s14, 0xfffffe00
	s_mul_hi_u32 s1, s0, 0x3e0f83e1
	s_lshr_b32 s23, s1, 8
	s_mul_i32 s22, s23, 0xfffffbe0
	s_add_i32 s22, s22, s0
	s_cmpk_gt_i32 s22, 0x15f
	s_mul_hi_u32 s27, s23, 0x2c00000
	s_mul_i32 s30, s23, 0x2c00000
	s_mov_b64 s[0:1], -1
	s_cbranch_scc0 .Lpc_455
	s_mov_b64 s[72:73], -1
	s_cmpk_gt_u32 s22, 0x2bf
	s_cbranch_scc0 .Lpc_453
	s_add_i32 s18, s22, 0xfffffd40
	v_readlane_b32 s0, v254, 49
	v_readlane_b32 s1, v254, 50
	s_add_u32 s46, s0, s30
	s_addc_u32 s47, s1, s27
	s_mul_i32 s1, s23, 0xb00000
	v_readlane_b32 s2, v254, 58
	s_mul_hi_u32 s0, s23, 0xb00000
	s_add_u32 s66, s2, s1
	v_readlane_b32 s1, v254, 59
	s_addc_u32 s67, s1, s0
	s_mov_b64 s[0:1], 0

.Lpc_461:
	s_lshr_b32 s0, s44, 8
	v_cvt_f32_u32_e32 v0, s0
	s_sub_i32 s23, 0, s0
	s_abs_i32 s22, s18
	s_ashr_i32 s1, s18, 31
	v_rcp_iflag_f32_e32 v0, v0
	v_lshlrev_b32_e32 v2, 2, v132
	v_ashrrev_i32_e32 v3, 31, v2
	s_mov_b32 s45, s90
	v_mul_f32_e32 v0, 0x4f7ffffe, v0
	v_cvt_u32_f32_e32 v0, v0
	s_nop 0
	v_readfirstlane_b32 s27, v0
	s_mul_i32 s23, s23, s27
	s_mul_hi_u32 s23, s27, s23
	s_add_i32 s27, s27, s23
	s_mul_hi_u32 s23, s22, s27
	s_mul_i32 s27, s23, s0
	s_sub_i32 s22, s22, s27
	s_add_i32 s27, s23, 1
	s_sub_i32 s30, s22, s0
	s_cmp_ge_u32 s22, s0
	s_cselect_b32 s23, s27, s23
	s_cselect_b32 s22, s30, s22
	s_add_i32 s27, s23, 1
	s_cmp_ge_u32 s22, s0
	s_cselect_b32 s22, s27, s23
	s_xor_b32 s22, s22, s1
	s_sub_i32 s1, s22, s1
	s_lshl_b32 s56, s1, 7
	s_mul_i32 s0, s1, s0
	s_add_i32 s1, s56, s96
	s_sub_i32 s0, s18, s0
	s_ashr_i32 s18, s1, 31
	s_mul_i32 s18, s18, s44
	s_mul_hi_u32 s22, s1, s44
	s_add_i32 s23, s22, s18
	s_mul_i32 s22, s1, s44
	s_lshl_b64 s[22:23], s[22:23], 2
	s_add_u32 s18, s46, s22
	s_addc_u32 s22, s47, s23
	s_lshl_b32 s84, s0, 8
	s_ashr_i32 s85, s84, 31
	s_lshl_b64 s[0:1], s[84:85], 2
	s_add_u32 s0, s18, s0
	s_addc_u32 s1, s22, s1
	v_lshl_add_u64 v[4:5], v[2:3], 2, s[0:1]
	v_lshl_add_u64 v[6:7], s[44:45], 2, v[4:5]
	s_lshl_b32 s0, s44, 1
	s_mov_b32 s1, s90
	global_load_dwordx4 v[66:69], v[4:5], off nt
	global_load_dwordx4 v[70:73], v[6:7], off nt
	v_lshl_add_u64 v[6:7], s[0:1], 2, v[4:5]
	s_mul_i32 s0, s44, 3
	global_load_dwordx4 v[74:77], v[6:7], off nt
	v_lshl_add_u64 v[6:7], s[0:1], 2, v[4:5]
	s_lshl_b32 s0, s44, 2
	global_load_dwordx4 v[78:81], v[6:7], off nt
	v_lshl_add_u64 v[6:7], s[0:1], 2, v[4:5]
	s_mul_i32 s0, s44, 5
	global_load_dwordx4 v[82:85], v[6:7], off nt
	v_lshl_add_u64 v[6:7], s[0:1], 2, v[4:5]
	s_mul_i32 s0, s44, 6
	global_load_dwordx4 v[86:89], v[6:7], off nt
	v_lshl_add_u64 v[6:7], s[0:1], 2, v[4:5]
	s_mul_i32 s0, s44, 7
	global_load_dwordx4 v[90:93], v[6:7], off nt
	v_lshl_add_u64 v[6:7], s[0:1], 2, v[4:5]
	s_lshl_b32 s0, s44, 3
	global_load_dwordx4 v[94:97], v[6:7], off nt
	v_lshl_add_u64 v[6:7], s[0:1], 2, v[4:5]
	s_mul_i32 s0, s44, 9
	global_load_dwordx4 v[98:101], v[6:7], off nt
	v_lshl_add_u64 v[6:7], s[0:1], 2, v[4:5]
	s_mul_i32 s0, s44, 10
	global_load_dwordx4 v[102:105], v[6:7], off nt
	v_lshl_add_u64 v[6:7], s[0:1], 2, v[4:5]
	s_mul_i32 s0, s44, 11
	global_load_dwordx4 v[106:109], v[6:7], off nt
	v_lshl_add_u64 v[6:7], s[0:1], 2, v[4:5]
	s_mul_i32 s0, s44, 12
	global_load_dwordx4 v[110:113], v[6:7], off nt
	v_lshl_add_u64 v[6:7], s[0:1], 2, v[4:5]
	s_mul_i32 s0, s44, 13
	global_load_dwordx4 v[114:117], v[6:7], off nt
	v_lshl_add_u64 v[6:7], s[0:1], 2, v[4:5]
	s_mul_i32 s0, s44, 14
	global_load_dwordx4 v[118:121], v[6:7], off nt
	v_lshl_add_u64 v[6:7], s[0:1], 2, v[4:5]
	s_mul_i32 s0, s44, 15
	v_lshl_add_u64 v[4:5], s[0:1], 2, v[4:5]
	global_load_dwordx4 v[122:125], v[6:7], off nt
	global_load_dwordx4 v[126:129], v[4:5], off nt
	s_branch .Lpipe_xc_done

; __device__ __forceinline__ CvTile cv_decode(const Ptrs& P, int it) {
;     constexpr int T_IN = (D / 128) * (NQKV / 256), T_O = (D / 128) * (D / 256), T_G = (D / 128) * (FF / 256), T_D = (FF / 128) * (D / 256), T_E = 2 * T_G + T_D;
;     CvTile c; int r = it; c.gain = nullptr; c.pitch = 0;
;     if (r < T_IN) { c.W = P.w_in; c.WT = (unsigned char*)P.Wqkv_t; c.K = D; c.N = NQKV; c.mode = 0; c.f8 = 0; c.r = r; return c; } r -= T_IN;
;     if (r < T_O) { c.W = P.w_out; c.WT = (unsigned char*)P.Wo_t; c.K = D; c.N = D; c.mode = 0; c.f8 = (WO8_LAYER == 0) ? 1 : 0; c.r = r; return c; } r -= T_O;
;     if (r < T_G) { c.W = P.dwg; c.WT = P.Wgu_d; c.K = D; c.N = FF; c.mode = 1; c.f8 = 1; c.r = r; return c; } r -= T_G;
;     if (r < T_G) { c.W = P.dwu; c.WT = P.Wgu_d; c.K = D; c.N = FF; c.mode = 2; c.f8 = 1; c.r = r; return c; } r -= T_G;
;     if (r < T_D) { c.W = P.dwd; c.WT = P.Wd_d; c.K = FF; c.N = D; c.mode = 0; c.f8 = 1; c.r = r; return c; } r -= T_D;
;     if (r < T_IN) { const int kb = r / 24, nb = r - kb * 24; c.K = D; c.mode = 0; c.pitch = NQKV; c.gain = P.attn_norm + D;
;         c.W = P.w_in + (size_t)D * NQKV; c.WT = P.Wv8; c.N = NQKV; c.f8 = 1; c.r = kb * 24 + nb;
;         return c; } r -= T_IN;
;     if (r < T_O) { c.W = P.w_out + (size_t)D * D; c.WT = (unsigned char*)(P.Wo_t + (size_t)D * D); c.K = D; c.N = D; c.mode = 0; c.f8 = (WO8_LAYER == 1) ? 1 : 0; c.r = r; return c; } r -= T_O;
;     const int e = r / T_E; r -= e * T_E; c.f8 = 1;
;     if (r < T_G) { c.W = P.mwg + (size_t)e * D * FF; c.WT = P.Wgu_m + (size_t)e * NGU * D; c.K = D; c.N = FF; c.mode = 1; c.r = r; return c; } r -= T_G;
;     if (r < T_G) { c.W = P.mwu + (size_t)e * D * FF; c.WT = P.Wgu_m + (size_t)e * NGU * D; c.K = D; c.N = FF; c.mode = 2; c.r = r; return c; } r -= T_G;
;     c.W = P.mwd + (size_t)e * FF * D; c.WT = P.Wd_m + (size_t)e * D * FF; c.K = FF; c.N = D; c.mode = 0; c.r = r; return c;
; __device__ __forceinline__ void convert_weights(const Ptrs& P, LAS unsigned char* lds, int t0, int step, int t1, int wave, int lane) {
;     ...
;     int ta = t0, tb = t0 + step, par = 0;
;     CvTile ca = cv_decode(P, ta), cb = ca; CV_LOAD(va, ca);
;     if (tb < t1) { cb = cv_decode(P, tb); CV_LOAD(vb, cb); }
.Lpipe_xc_done:
	s_and_b64 vcc, exec, s[42:43]
	s_cbranch_vccz .Lpd_473
	s_cmpk_gt_u32 s15, 0xff
	s_mov_b64 s[0:1], -1
	s_cbranch_scc0 .Lpd_471
	s_add_i32 s0, s14, 0xfffffe01
	s_mul_hi_u32 s1, s0, 0x3e0f83e1
	s_lshr_b32 s23, s1, 8
	s_mul_i32 s15, s23, 0xfffffbe0
	s_add_i32 s15, s15, s0
	s_cmpk_gt_i32 s15, 0x15f
	s_mul_hi_u32 s27, s23, 0x2c00000
	s_mul_i32 s28, s23, 0x2c00000
	s_mov_b64 s[0:1], -1
	s_cbranch_scc0 .Lpd_468
	s_mov_b64 s[62:63], -1
	s_cmpk_gt_u32 s15, 0x2bf
	s_cbranch_scc0 .Lpd_466
	s_add_i32 s22, s15, 0xfffffd40
	v_readlane_b32 s0, v254, 49
	v_readlane_b32 s1, v254, 50
	s_add_u32 s44, s0, s28
	s_addc_u32 s45, s1, s27
	s_mul_i32 s1, s23, 0xb00000
	v_readlane_b32 s2, v254, 58
	s_mul_hi_u32 s0, s23, 0xb00000
	s_add_u32 s58, s2, s1
	v_readlane_b32 s1, v254, 59
	s_addc_u32 s59, s1, s0
	s_mov_b64 s[0:1], 0

.Lpd_475:
	s_lshr_b32 s0, s42, 8
	v_cvt_f32_u32_e32 v0, s0
	s_sub_i32 s15, 0, s0
	s_abs_i32 s14, s22
	s_ashr_i32 s1, s22, 31
	v_rcp_iflag_f32_e32 v0, v0
	s_mov_b32 s43, s90
	v_mul_f32_e32 v0, 0x4f7ffffe, v0
	v_cvt_u32_f32_e32 v0, v0
	s_nop 0
	v_readfirstlane_b32 s23, v0
	s_mul_i32 s15, s15, s23
	s_mul_hi_u32 s15, s23, s15
	s_add_i32 s23, s23, s15
	s_mul_hi_u32 s15, s14, s23
	s_mul_i32 s23, s15, s0
	s_sub_i32 s14, s14, s23
	s_add_i32 s23, s15, 1
	s_sub_i32 s27, s14, s0
	s_cmp_ge_u32 s14, s0
	s_cselect_b32 s15, s23, s15
	s_cselect_b32 s14, s27, s14
	s_add_i32 s23, s15, 1
	s_cmp_ge_u32 s14, s0
	s_cselect_b32 s14, s23, s15
	s_xor_b32 s14, s14, s1
	s_sub_i32 s1, s14, s1
	s_lshl_b32 s70, s1, 7
	s_mul_i32 s0, s1, s0
	s_add_i32 s1, s70, s96
	s_ashr_i32 s14, s1, 31
	s_mul_i32 s14, s14, s42
	s_mul_hi_u32 s15, s1, s42
	s_add_i32 s15, s15, s14
	s_mul_i32 s14, s1, s42
	s_sub_i32 s0, s22, s0
	s_lshl_b64 s[14:15], s[14:15], 2
	s_add_u32 s14, s44, s14
	s_addc_u32 s15, s45, s15
	s_lshl_b32 s64, s0, 8
	s_ashr_i32 s65, s64, 31
	s_lshl_b64 s[0:1], s[64:65], 2
	s_add_u32 s0, s14, s0
	s_addc_u32 s1, s15, s1
	v_lshl_add_u64 v[62:63], v[2:3], 2, s[0:1]
	s_lshl_b32 s0, s42, 1
	s_mov_b32 s1, s90
	v_lshl_add_u64 v[10:11], s[0:1], 2, v[62:63]
	s_mul_i32 s0, s42, 3
	v_lshl_add_u64 v[14:15], s[0:1], 2, v[62:63]
	s_lshl_b32 s0, s42, 2
	v_lshl_add_u64 v[18:19], s[0:1], 2, v[62:63]
	s_mul_i32 s0, s42, 5
	v_lshl_add_u64 v[22:23], s[0:1], 2, v[62:63]
	s_mul_i32 s0, s42, 6
	v_lshl_add_u64 v[26:27], s[0:1], 2, v[62:63]
	s_mul_i32 s0, s42, 7
	v_lshl_add_u64 v[30:31], s[0:1], 2, v[62:63]
	s_lshl_b32 s0, s42, 3
	v_lshl_add_u64 v[34:35], s[0:1], 2, v[62:63]
	s_mul_i32 s0, s42, 9
	v_lshl_add_u64 v[38:39], s[0:1], 2, v[62:63]
	s_mul_i32 s0, s42, 10
	v_lshl_add_u64 v[42:43], s[0:1], 2, v[62:63]
	s_mul_i32 s0, s42, 11
	v_lshl_add_u64 v[46:47], s[0:1], 2, v[62:63]
	s_mul_i32 s0, s42, 12
	v_lshl_add_u64 v[50:51], s[0:1], 2, v[62:63]
	s_mul_i32 s0, s42, 13
	v_lshl_add_u64 v[54:55], s[0:1], 2, v[62:63]
	s_mul_i32 s0, s42, 14
	v_lshl_add_u64 v[58:59], s[0:1], 2, v[62:63]
	s_mul_i32 s0, s42, 15
	global_load_dwordx4 v[2:5], v[62:63], off nt
	v_lshl_add_u64 v[6:7], s[42:43], 2, v[62:63]
	v_lshl_add_u64 v[62:63], s[0:1], 2, v[62:63]
	global_load_dwordx4 v[6:9], v[6:7], off nt
	s_cmp_eq_u64 s[40:41], 0
	global_load_dwordx4 v[10:13], v[10:11], off nt
	s_nop 0
	global_load_dwordx4 v[14:17], v[14:15], off nt
	s_nop 0
	global_load_dwordx4 v[18:21], v[18:19], off nt
	s_nop 0
	global_load_dwordx4 v[22:25], v[22:23], off nt
	s_nop 0
	global_load_dwordx4 v[26:29], v[26:27], off nt
	s_nop 0
	global_load_dwordx4 v[30:33], v[30:31], off nt
	s_nop 0
	global_load_dwordx4 v[34:37], v[34:35], off nt
	s_nop 0
	global_load_dwordx4 v[38:41], v[38:39], off nt
	s_nop 0
	global_load_dwordx4 v[42:45], v[42:43], off nt
	s_nop 0
	global_load_dwordx4 v[46:49], v[46:47], off nt
	s_nop 0
	global_load_dwordx4 v[50:53], v[50:51], off nt
	s_nop 0
	global_load_dwordx4 v[54:57], v[54:55], off nt
	s_nop 0
	global_load_dwordx4 v[58:61], v[58:59], off nt
	s_nop 0
	global_load_dwordx4 v[62:65], v[62:63], off nt
	s_branch .Lpipe_xd_done

.Lpipe_xd_done:
	s_cbranch_scc1 .Lpa2_477
	s_ashr_i32 s57, s56, 31
	s_lshl_b64 s[0:1], s[56:57], 2
	s_add_u32 s0, s40, s0
	s_addc_u32 s1, s41, s1
	s_lshl_b32 s14, s96, 2
	s_load_dwordx16 s[40:55], s[0:1], s14 offset:0x0
	s_waitcnt lgkmcnt(0)
	s_mov_b32 s0, s43
	s_waitcnt vmcnt(28)
	v_pk_mul_f32 v[80:81], v[80:81], s[0:1] op_sel_hi:[1,0]
	v_pk_mul_f32 v[78:79], v[78:79], s[0:1] op_sel_hi:[1,0]
	s_mov_b32 s0, s45
	s_waitcnt vmcnt(26)
	v_pk_mul_f32 v[88:89], v[88:89], s[0:1] op_sel_hi:[1,0]
	v_pk_mul_f32 v[86:87], v[86:87], s[0:1] op_sel_hi:[1,0]
	s_mov_b32 s0, s47
	s_waitcnt vmcnt(24)
	v_pk_mul_f32 v[96:97], v[96:97], s[0:1] op_sel_hi:[1,0]
	v_pk_mul_f32 v[94:95], v[94:95], s[0:1] op_sel_hi:[1,0]
	s_mov_b32 s0, s49
	s_waitcnt vmcnt(22)
	v_pk_mul_f32 v[104:105], v[104:105], s[0:1] op_sel_hi:[1,0]
	v_pk_mul_f32 v[102:103], v[102:103], s[0:1] op_sel_hi:[1,0]
	s_mov_b32 s0, s51
	s_waitcnt vmcnt(20)
	v_pk_mul_f32 v[112:113], v[112:113], s[0:1] op_sel_hi:[1,0]
	v_pk_mul_f32 v[110:111], v[110:111], s[0:1] op_sel_hi:[1,0]
	s_mov_b32 s0, s53
	s_waitcnt vmcnt(18)
	v_pk_mul_f32 v[120:121], v[120:121], s[0:1] op_sel_hi:[1,0]
	v_pk_mul_f32 v[118:119], v[118:119], s[0:1] op_sel_hi:[1,0]
	s_mov_b32 s0, s55
	v_pk_mul_f32 v[68:69], v[68:69], s[40:41] op_sel_hi:[1,0]
	v_pk_mul_f32 v[66:67], v[66:67], s[40:41] op_sel_hi:[1,0]
	v_pk_mul_f32 v[72:73], v[72:73], s[40:41] op_sel:[0,1]
	v_pk_mul_f32 v[70:71], v[70:71], s[40:41] op_sel:[0,1]
	v_pk_mul_f32 v[76:77], v[76:77], s[42:43] op_sel_hi:[1,0]
	v_pk_mul_f32 v[74:75], v[74:75], s[42:43] op_sel_hi:[1,0]
	v_pk_mul_f32 v[84:85], v[84:85], s[44:45] op_sel_hi:[1,0]
	v_pk_mul_f32 v[82:83], v[82:83], s[44:45] op_sel_hi:[1,0]
	v_pk_mul_f32 v[92:93], v[92:93], s[46:47] op_sel_hi:[1,0]
	v_pk_mul_f32 v[90:91], v[90:91], s[46:47] op_sel_hi:[1,0]
	v_pk_mul_f32 v[100:101], v[100:101], s[48:49] op_sel_hi:[1,0]
	v_pk_mul_f32 v[98:99], v[98:99], s[48:49] op_sel_hi:[1,0]
	v_pk_mul_f32 v[108:109], v[108:109], s[50:51] op_sel_hi:[1,0]
	v_pk_mul_f32 v[106:107], v[106:107], s[50:51] op_sel_hi:[1,0]
	v_pk_mul_f32 v[116:117], v[116:117], s[52:53] op_sel_hi:[1,0]
	v_pk_mul_f32 v[114:115], v[114:115], s[52:53] op_sel_hi:[1,0]
	s_waitcnt vmcnt(17)
	v_pk_mul_f32 v[124:125], v[124:125], s[54:55] op_sel_hi:[1,0]
	v_pk_mul_f32 v[122:123], v[122:123], s[54:55] op_sel_hi:[1,0]
	s_waitcnt vmcnt(16)
	v_pk_mul_f32 v[128:129], v[128:129], s[0:1] op_sel_hi:[1,0]
	v_pk_mul_f32 v[126:127], v[126:127], s[0:1] op_sel_hi:[1,0]

_ZN3attL9ATT_ORDERE:
	.short	8207
	.short	8206
	.short	8205
	.short	8204
	.short	8203
	.short	8202
	.short	8201
	.short	8200
	.short	8199
	.short	8198
	.short	8197
	.short	8196
	.short	8195
	.short	8194
	.short	8193
	.short	8271
	.short	8270
	.short	8269
	.short	8268
	.short	8267
	.short	8266
	.short	8265
	.short	8264
	.short	8263
	.short	8262
	.short	8261
	.short	8260
	.short	8259
	.short	8258
	.short	8257
	.short	8335
	.short	8334
	.short	8333
	.short	8332
	.short	8331
	.short	8330
	.short	8329
	.short	8328
	.short	8327
	.short	8326
	.short	8325
	.short	8324
	.short	8323
	.short	8322
	.short	8321
	.short	8399
	.short	8398
	.short	8397
	.short	8396
	.short	8395
	.short	8394
	.short	8393
	.short	8392
	.short	8391
	.short	8390
	.short	8389
	.short	8388
	.short	8387
	.short	8386
	.short	8385
	.short	8463
	.short	8462
	.short	8461
	.short	8460
	.short	8459
	.short	8458
	.short	8457
	.short	8456
	.short	8455
	.short	8454
	.short	8453
	.short	8452
	.short	8451
	.short	8450
	.short	8449
	.short	8719
	.short	8718
	.short	8717
	.short	8716
	.short	8715
	.short	8714
	.short	8713
	.short	8712
	.short	8711
	.short	8710
	.short	8709
	.short	8708
	.short	8707
	.short	8706
	.short	8705
	.short	8783
	.short	8782
	.short	8781
	.short	8780
	.short	8779
	.short	8778
	.short	8777
	.short	8776
	.short	8775
	.short	8774
	.short	8773
	.short	8772
	.short	8771
	.short	8770
	.short	8769
	.short	8847
	.short	8846
	.short	8845
	.short	8844
	.short	8843
	.short	8842
	.short	8841
	.short	8840
	.short	8839
	.short	8838
	.short	8837
	.short	8836
	.short	8835
	.short	8834
	.short	8833
	.short	8911
	.short	8910
	.short	8909
	.short	8908
	.short	8907
	.short	8906
	.short	8905
	.short	8904
	.short	8903
	.short	8902
	.short	8901
	.short	8900
	.short	8899
	.short	8898
	.short	8897
	.short	8975
	.short	8974
	.short	8973
	.short	8972
	.short	8971
	.short	8970
	.short	8969
	.short	8968
	.short	8967
	.short	8966
	.short	8965
	.short	8964
	.short	8963
	.short	8962
	.short	8961
	.short	2063
	.short	32768
	.short	2127
	.short	32769
	.short	2191
	.short	32770
	.short	2255
	.short	32771
	.short	2319
	.short	32772
	.short	2575
	.short	32773
	.short	2639
	.short	32774
	.short	32775
	.short	2703
	.short	32776
	.short	2767
	.short	32777
	.short	2831
	.short	32778
	.short	2062
	.short	32779
	.short	2126
	.short	32780
	.short	2190
	.short	32781
	.short	2254
	.short	32782
	.short	2318
	.short	32783
	.short	2574
	.short	32784
	.short	2638
	.short	32785
	.short	2702
	.short	32786
	.short	2766
	.short	32787
	.short	2830
	.short	32788
	.short	32789
	.short	2061
	.short	32790
	.short	2125
	.short	32791
	.short	2189
	.short	32792
	.short	2253
	.short	32793
	.short	2317
	.short	32794
	.short	2573
	.short	32795
	.short	2637
	.short	32796
	.short	2701
	.short	32797
	.short	2765
	.short	32798
	.short	2829
	.short	32799
	.short	2060
	.short	32800
	.short	2124
	.short	32801
	.short	2188
	.short	32802
	.short	32803
	.short	2252
	.short	32804
	.short	2316
	.short	32805
	.short	2572
	.short	32806
	.short	2636
	.short	32807
	.short	2700
	.short	32808
	.short	2764
	.short	32809
	.short	2828
	.short	32810
	.short	2059
	.short	32811
	.short	2123
	.short	32812
	.short	2187
	.short	32813
	.short	2251
	.short	32814
	.short	2315
	.short	32815
	.short	2571
	.short	32816
	.short	32817
	.short	2635
	.short	32818
	.short	2699
	.short	32819
	.short	2763
	.short	32820
	.short	2827
	.short	32821
	.short	2058
	.short	32822
	.short	2122
	.short	32823
	.short	2186
	.short	32824
	.short	2250
	.short	32825
	.short	2314
	.short	32826
	.short	2570
	.short	32827
	.short	2634
	.short	32828
	.short	2698
	.short	32829
	.short	2762
	.short	32830
	.short	32831
	.short	2826
	.short	32832
	.short	2057
	.short	32833
	.short	2121
	.short	32834
	.short	2185
	.short	32835
	.short	2249
	.short	32836
	.short	2313
	.short	32837
	.short	2569
	.short	32838
	.short	2633
	.short	32839
	.short	2697
	.short	32840
	.short	2761
	.short	32841
	.short	2825
	.short	32842
	.short	2056
	.short	32843
	.short	2120
	.short	32844
	.short	32845
	.short	2184
	.short	32846
	.short	2248
	.short	32847
	.short	2312
	.short	32848
	.short	2568
	.short	32849
	.short	2632
	.short	32850
	.short	2696
	.short	32851
	.short	2760
	.short	32852
	.short	2824
	.short	32853
	.short	2055
	.short	32854
	.short	2119
	.short	32855
	.short	2183
	.short	32856
	.short	2247
	.short	32857
	.short	2311
	.short	32858
	.short	32859
	.short	2567
	.short	32860
	.short	2631
	.short	32861
	.short	2695
	.short	32862
	.short	2759
	.short	32863
	.short	2823
	.short	32864
	.short	2054
	.short	32865
	.short	2118
	.short	32866
	.short	2182
	.short	32867
	.short	2246
	.short	32868
	.short	2310
	.short	32869
	.short	2566
	.short	32870
	.short	2630
	.short	32871
	.short	2694
	.short	32872
	.short	32873
	.short	2758
	.short	32874
	.short	2822
	.short	32875
	.short	2053
	.short	32876
	.short	2117
	.short	32877
	.short	2181
	.short	32878
	.short	2245
	.short	32879
	.short	2309
	.short	32880
	.short	2565
	.short	32881
	.short	2629
	.short	32882
	.short	2693
	.short	32883
	.short	2757
	.short	32884
	.short	2821
	.short	32885
	.short	2052
	.short	32886
	.short	32887
	.short	2116
	.short	32888
	.short	2180
	.short	32889
	.short	2244
	.short	32890
	.short	2308
	.short	32891
	.short	2564
	.short	32892
	.short	2628
	.short	32893
	.short	2692
	.short	32894
	.short	2756
	.short	32895
	.short	2820
	.short	32896
	.short	2051
	.short	32897
	.short	2115
	.short	32898
	.short	2179
	.short	32899
	.short	2243
	.short	32900
	.short	32901
	.short	2307
	.short	32902
	.short	2563
	.short	32903
	.short	2627
	.short	32904
	.short	2691
	.short	32905
	.short	2755
	.short	32906
	.short	2819
	.short	32907
	.short	2050
	.short	32908
	.short	2114
	.short	32909
	.short	2178
	.short	32910
	.short	2242
	.short	32911
	.short	2306
	.short	32912
	.short	2562
	.short	32913
	.short	2626
	.short	32914
	.short	32915
	.short	2690
	.short	32916
	.short	2754
	.short	32917
	.short	2818
	.short	32918
	.short	2049
	.short	32919
	.short	2113
	.short	32920
	.short	2177
	.short	32921
	.short	2241
	.short	32922
	.short	2305
	.short	32923
	.short	2561
	.short	32924
	.short	2625
	.short	32925
	.short	2689
	.short	32926
	.short	2753
	.short	32927
	.short	2817
	.short	32928
	.short	32929
	.short	2048
	.short	2112
	.short	32930
	.short	2176
	.short	32931
	.short	2240
	.short	2304
	.short	32932
	.short	2560
	.short	32933
	.short	2624
	.short	32934
	.short	2688
	.short	2752
	.short	32935
	.short	2816
	.short	32936
	.short	1039
	.short	1103
	.short	32937
	.short	1167
	.short	32938
	.short	1231
	.short	32939
	.short	1295
	.short	1551
	.short	32940
	.short	1615
	.short	32941
	.short	1679
	.short	1743
	.short	32942
	.short	1807
	.short	32943
	.short	1038
	.short	32944
	.short	1102
	.short	1166
	.short	32945
	.short	1230
	.short	32946
	.short	1294
	.short	1550
	.short	32947
	.short	1614
	.short	32948
	.short	1678
	.short	32949
	.short	1742
	.short	1806
	.short	32950
	.short	1037
	.short	32951
	.short	1101
	.short	1165
	.short	32952
	.short	1229
	.short	32953
	.short	1293
	.short	32954
	.short	1549
	.short	1613
	.short	32955
	.short	1677
	.short	32956
	.short	1741
	.short	32957
	.short	1805
	.short	1036
	.short	32958
	.short	1100
	.short	32959
	.short	1164
	.short	1228
	.short	32960
	.short	1292
	.short	32961
	.short	1548
	.short	32962
	.short	1612
	.short	1676
	.short	32963
	.short	1740
	.short	32964
	.short	1804
	.short	1035
	.short	32965
	.short	1099
	.short	32966
	.short	1163
	.short	32967
	.short	1227
	.short	1291
	.short	32968
	.short	1547
	.short	32969
	.short	1611
	.short	1675
	.short	32970
	.short	1739
	.short	32971
	.short	1803
	.short	32972
	.short	1034
	.short	1098
	.short	32973
	.short	1162
	.short	32974
	.short	1226
	.short	1290
	.short	32975
	.short	1546
	.short	32976
	.short	1610
	.short	32977
	.short	1674
	.short	1738
	.short	32978
	.short	1802
	.short	32979
	.short	1033
	.short	1097
	.short	32980
	.short	1161
	.short	32981
	.short	1225
	.short	32982
	.short	1289
	.short	1545
	.short	32983
	.short	1609
	.short	32984
	.short	1673
	.short	32985
	.short	1737
	.short	1801
	.short	32986
	.short	1032
	.short	32987
	.short	1096
	.short	1160
	.short	32988
	.short	1224
	.short	32989
	.short	1288
	.short	32990
	.short	1544
	.short	1608
	.short	32991
	.short	1672
	.short	32992
	.short	1736
	.short	1800
	.short	32993
	.short	1031
	.short	32994
	.short	1095
	.short	32995
	.short	1159
	.short	1223
	.short	32996
	.short	1287
	.short	32997
	.short	1543
	.short	1607
	.short	32998
	.short	1671
	.short	32999
	.short	1735
	.short	33000
	.short	1799
	.short	1030
	.short	33001
	.short	1094
	.short	33002
	.short	1158
	.short	1222
	.short	33003
	.short	1286
	.short	33004
	.short	1542
	.short	33005
	.short	1606
	.short	1670
	.short	33006
	.short	1734
	.short	33007
	.short	1798
	.short	1029
	.short	33008
	.short	1093
	.short	33009
	.short	1157
	.short	33010
	.short	1221
	.short	1285
	.short	33011
	.short	1541
	.short	33012
	.short	1605
	.short	33013
	.short	1669
	.short	1733
	.short	33014
	.short	1797
	.short	33015
	.short	1028
	.short	1092
	.short	33016
	.short	1156
	.short	33017
	.short	1220
	.short	33018
	.short	1284
	.short	1540
	.short	33019
	.short	1604
	.short	33020
	.short	1668
	.short	1732
	.short	33021
	.short	1796
	.short	33022
	.short	1027
	.short	33023
	.short	1091
	.short	1155
	.short	33024
	.short	1219
	.short	33025
	.short	1283
	.short	1539
	.short	33026
	.short	1603
	.short	33027
	.short	1667
	.short	33028
	.short	1731
	.short	1795
	.short	33029
	.short	1026
	.short	33030
	.short	1090
	.short	1154
	.short	33031
	.short	1218
	.short	33032
	.short	1282
	.short	33033
	.short	1538
	.short	1602
	.short	33034
	.short	1666
	.short	33035
	.short	1730
	.short	1794
	.short	33036
	.short	1025
	.short	33037
	.short	1089
	.short	33038
	.short	1153
	.short	1217
	.short	33039
	.short	1281
	.short	33040
	.short	1537
	.short	33041
	.short	1601
	.short	1665
	.short	33042
	.short	1729
	.short	33043
	.short	1793
	.short	1024
	.short	33044
	.short	1088
	.short	33045
	.short	1152
	.short	33046
	.short	1216
	.short	1280
	.short	33047
	.short	1536
	.short	33048
	.short	1600
	.short	1664
	.short	33049
	.short	1728
	.short	33050
	.short	1792
	.short	33051
	.short	47
	.short	111
	.short	33052
	.short	175
	.short	33053
	.short	239
	.short	303
	.short	33054
	.short	367
	.short	33055
	.short	559
	.short	33056
	.short	623
	.short	687
	.short	33057
	.short	751
	.short	33058
	.short	815
	.short	879
	.short	33059
	.short	46
	.short	33060
	.short	110
	.short	33061
	.short	174
	.short	238
	.short	33062
	.short	302
	.short	33063
	.short	366
	.short	558
	.short	33064
	.short	622
	.short	33065
	.short	686
	.short	33066
	.short	750
	.short	814
	.short	33067
	.short	878
	.short	33068
	.short	45
	.short	33069
	.short	109
	.short	173
	.short	33070
	.short	237
	.short	33071
	.short	301
	.short	365
	.short	33072
	.short	557
	.short	33073
	.short	621
	.short	33074
	.short	685
	.short	749
	.short	33075
	.short	813
	.short	33076
	.short	877
	.short	44
	.short	33077
	.short	108
	.short	33078
	.short	172
	.short	33079
	.short	236
	.short	300
	.short	33080
	.short	364
	.short	33081
	.short	556
	.short	620
	.short	33082
	.short	684
	.short	33083
	.short	748
	.short	33084
	.short	812
	.short	876
	.short	33085
	.short	43
	.short	33086
	.short	107
	.short	171
	.short	33087
	.short	235
	.short	33088
	.short	299
	.short	33089
	.short	363
	.short	555
	.short	33090
	.short	619
	.short	33091
	.short	683
	.short	747
	.short	33092
	.short	811
	.short	33093
	.short	875
	.short	33094
	.short	42
	.short	106
	.short	33095
	.short	170
	.short	33096
	.short	234
	.short	33097
	.short	298
	.short	362
	.short	33098
	.short	554
	.short	33099
	.short	618
	.short	682
	.short	33100
	.short	746
	.short	33101
	.short	810
	.short	33102
	.short	874
	.short	41
	.short	33103
	.short	105
	.short	33104
	.short	169
	.short	233
	.short	33105
	.short	297
	.short	33106
	.short	361
	.short	33107
	.short	553
	.short	617
	.short	33108
	.short	681
	.short	33109
	.short	745
	.short	809
	.short	33110
	.short	873
	.short	33111
	.short	40
	.short	33112
	.short	104
	.short	168
	.short	33113
	.short	232
	.short	33114
	.short	296
	.short	360
	.short	33115
	.short	552
	.short	33116
	.short	616
	.short	33117
	.short	680
	.short	744
	.short	33118
	.short	808
	.short	33119
	.short	872
	.short	39
	.short	33120
	.short	103
	.short	33121
	.short	167
	.short	33122
	.short	231
	.short	295
	.short	33123
	.short	359
	.short	33124
	.short	551
	.short	33125
	.short	615
	.short	679
	.short	33126
	.short	743
	.short	33127
	.short	807
	.short	871
	.short	33128
	.short	38
	.short	33129
	.short	102
	.short	33130
	.short	166
	.short	230
	.short	33131
	.short	294
	.short	33132
	.short	358
	.short	550
	.short	33133
	.short	614
	.short	33134
	.short	678
	.short	33135
	.short	742
	.short	806
	.short	33136
	.short	870
	.short	33137
	.short	37
	.short	101
	.short	33138
	.short	165
	.short	33139
	.short	229
	.short	33140
	.short	293
	.short	357
	.short	33141
	.short	549
	.short	33142
	.short	613
	.short	677
	.short	33143
	.short	741
	.short	33144
	.short	805
	.short	33145
	.short	869
	.short	36
	.short	33146
	.short	100
	.short	33147
	.short	164
	.short	228
	.short	33148
	.short	292
	.short	33149
	.short	356
	.short	33150
	.short	548
	.short	612
	.short	33151
	.short	676
	.short	33152
	.short	740
	.short	33153
	.short	804
	.short	868
	.short	33154
	.short	35
	.short	33155
	.short	99
	.short	163
	.short	33156
	.short	227
	.short	33157
	.short	291
	.short	33158
	.short	355
	.short	547
	.short	33159
	.short	611
	.short	33160
	.short	675
	.short	739
	.short	33161
	.short	803
	.short	33162
	.short	867
	.short	33163
	.short	34
	.short	98
	.short	33164
	.short	162
	.short	33165
	.short	226
	.short	290
	.short	33166
	.short	354
	.short	33167
	.short	546
	.short	33168
	.short	610
	.short	674
	.short	33169
	.short	738
	.short	33170
	.short	802
	.short	866
	.short	33171
	.short	33
	.short	33172
	.short	97
	.short	33173
	.short	161
	.short	225
	.short	33174
	.short	289
	.short	33175
	.short	353
	.short	545
	.short	33176
	.short	609
	.short	33177
	.short	673
	.short	33178
	.short	737
	.short	801
	.short	33179
	.short	865
	.short	33180
	.short	32
	.short	96
	.short	33181
	.short	160
	.short	33182
	.short	224
	.short	33183
	.short	288
	.short	352
	.short	33184
	.short	544
	.short	33185
	.short	608
	.short	33186
	.short	672
	.short	736
	.short	33187
	.short	800
	.short	33188
	.short	864
	.short	31
	.short	33189
	.short	95
	.short	33190
	.short	159
	.short	33191
	.short	223
	.short	287
	.short	33192
	.short	351
	.short	33193
	.short	543
	.short	607
	.short	33194
	.short	671
	.short	33195
	.short	735
	.short	33196
	.short	799
	.short	863
	.short	33197
	.short	30
	.short	33198
	.short	94
	.short	158
	.short	33199
	.short	222
	.short	33200
	.short	286
	.short	33201
	.short	350
	.short	542
	.short	33202
	.short	606
	.short	33203
	.short	670
	.short	734
	.short	33204
	.short	798
	.short	33205
	.short	862
	.short	33206
	.short	29
	.short	93
	.short	33207
	.short	157
	.short	33208
	.short	221
	.short	285
	.short	33209
	.short	349
	.short	33210
	.short	541
	.short	33211
	.short	605
	.short	669
	.short	33212
	.short	733
	.short	33213
	.short	797
	.short	33214
	.short	861
	.short	28
	.short	33215
	.short	92
	.short	33216
	.short	156
	.short	220
	.short	33217
	.short	284
	.short	33218
	.short	348
	.short	33219
	.short	540
	.short	604
	.short	33220
	.short	668
	.short	33221
	.short	732
	.short	796
	.short	33222
	.short	860
	.short	33223
	.short	27
	.short	33224
	.short	91
	.short	155
	.short	33225
	.short	219
	.short	33226
	.short	283
	.short	347
	.short	33227
	.short	539
	.short	33228
	.short	603
	.short	33229
	.short	667
	.short	731
	.short	33230
	.short	795
	.short	33231
	.short	859
	.short	26
	.short	33232
	.short	90
	.short	33233
	.short	154
	.short	33234
	.short	218
	.short	282
	.short	33235
	.short	346
	.short	33236
	.short	538
	.short	602
	.short	33237
	.short	666
	.short	33238
	.short	730
	.short	33239
	.short	794
	.short	858
	.short	33240
	.short	25
	.short	33241
	.short	89
	.short	33242
	.short	153
	.short	217
	.short	33243
	.short	281
	.short	33244
	.short	345
	.short	537
	.short	33245
	.short	601
	.short	33246
	.short	665
	.short	33247
	.short	729
	.short	793
	.short	33248
	.short	857
	.short	33249
	.short	24
	.short	88
	.short	33250
	.short	152
	.short	33251
	.short	216
	.short	33252
	.short	280
	.short	344
	.short	33253
	.short	536
	.short	33254
	.short	600
	.short	664
	.short	33255
	.short	728
	.short	33256
	.short	792
	.short	33257
	.short	856
	.short	23
	.short	33258
	.short	87
	.short	33259
	.short	151
	.short	215
	.short	33260
	.short	279
	.short	33261
	.short	343
	.short	33262
	.short	535
	.short	599
	.short	33263
	.short	663
	.short	33264
	.short	727
	.short	791
	.short	33265
	.short	855
	.short	33266
	.short	22
	.short	33267
	.short	86
	.short	150
	.short	33268
	.short	214
	.short	33269
	.short	278
	.short	33270
	.short	342
	.short	534
	.short	33271
	.short	598
	.short	33272
	.short	662
	.short	726
	.short	33273
	.short	790
	.short	33274
	.short	854
	.short	33275
	.short	21
	.short	85
	.short	33276
	.short	149
	.short	33277
	.short	213
	.short	277
	.short	33278
	.short	341
	.short	33279
	.short	533
	.short	33280
	.short	597
	.short	661
	.short	33281
	.short	725
	.short	33282
	.short	789
	.short	853
	.short	33283
	.short	20
	.short	33284
	.short	84
	.short	33285
	.short	148
	.short	212
	.short	33286
	.short	276
	.short	33287
	.short	340
	.short	532
	.short	33288
	.short	596
	.short	33289
	.short	660
	.short	33290
	.short	724
	.short	788
	.short	33291
	.short	852
	.short	33292
	.short	19
	.short	83
	.short	33293
	.short	147
	.short	33294
	.short	211
	.short	33295
	.short	275
	.short	339
	.short	33296
	.short	531
	.short	33297
	.short	595
	.short	33298
	.short	659
	.short	723
	.short	33299
	.short	787
	.short	33300
	.short	851
	.short	18
	.short	33301
	.short	82
	.short	33302
	.short	146
	.short	33303
	.short	210
	.short	274
	.short	33304
	.short	338
	.short	33305
	.short	530
	.short	594
	.short	33306
	.short	658
	.short	33307
	.short	722
	.short	33308
	.short	786
	.short	850
	.short	33309
	.short	17
	.short	33310
	.short	81
	.short	145
	.short	33311
	.short	209
	.short	33312
	.short	273
	.short	33313
	.short	337
	.short	529
	.short	33314
	.short	593
	.short	33315
	.short	657
	.short	721
	.short	33316
	.short	785
	.short	33317
	.short	849
	.short	33318
	.short	16
	.short	80
	.short	33319
	.short	144
	.short	33320
	.short	208
	.short	272
	.short	33321
	.short	336
	.short	33322
	.short	528
	.short	33323
	.short	592
	.short	656
	.short	33324
	.short	720
	.short	33325
	.short	784
	.short	33326
	.short	848
	.short	15
	.short	33327
	.short	79
	.short	33328
	.short	143
	.short	207
	.short	33329
	.short	271
	.short	33330
	.short	335
	.short	33331
	.short	527
	.short	591
	.short	33332
	.short	655
	.short	33333
	.short	719
	.short	783
	.short	33334
	.short	847
	.short	33335
	.short	14
	.short	33336
	.short	78
	.short	142
	.short	33337
	.short	206
	.short	33338
	.short	270
	.short	334
	.short	33339
	.short	526
	.short	33340
	.short	590
	.short	33341
	.short	654
	.short	718
	.short	33342
	.short	782
	.short	33343
	.short	846
	.short	13
	.short	33344
	.short	77
	.short	33345
	.short	141
	.short	33346
	.short	205
	.short	269
	.short	33347
	.short	333
	.short	33348
	.short	525
	.short	589
	.short	33349
	.short	653
	.short	33350
	.short	717
	.short	33351
	.short	781
	.short	845
	.short	33352
	.short	12
	.short	33353
	.short	76
	.short	33354
	.short	140
	.short	204
	.short	33355
	.short	268
	.short	33356
	.short	332
	.short	524
	.short	33357
	.short	588
	.short	33358
	.short	652
	.short	33359
	.short	716
	.short	780
	.short	33360
	.short	844
	.short	33361
	.short	11
	.short	75
	.short	33362
	.short	139
	.short	33363
	.short	203
	.short	33364
	.short	267
	.short	331
	.short	33365
	.short	523
	.short	33366
	.short	587
	.short	651
	.short	33367
	.short	715
	.short	33368
	.short	779
	.short	33369
	.short	843
	.short	10
	.short	33370
	.short	74
	.short	33371
	.short	138
	.short	202
	.short	33372
	.short	266
	.short	33373
	.short	330
	.short	33374
	.short	522
	.short	586
	.short	33375
	.short	650
	.short	33376
	.short	714
	.short	778
	.short	33377
	.short	842
	.short	33378
	.short	9
	.short	33379
	.short	73
	.short	137
	.short	33380
	.short	201
	.short	33381
	.short	265
	.short	33382
	.short	329
	.short	521
	.short	33383
	.short	585
	.short	33384
	.short	649
	.short	713
	.short	33385
	.short	777
	.short	33386
	.short	841
	.short	33387
	.short	8
	.short	72
	.short	33388
	.short	136
	.short	33389
	.short	200
	.short	264
	.short	33390
	.short	328
	.short	33391
	.short	520
	.short	33392
	.short	584
	.short	648
	.short	33393
	.short	712
	.short	33394
	.short	776
	.short	840
	.short	33395
	.short	7
	.short	33396
	.short	71
	.short	33397
	.short	135
	.short	199
	.short	33398
	.short	263
	.short	33399
	.short	327
	.short	519
	.short	33400
	.short	583
	.short	33401
	.short	647
	.short	33402
	.short	711
	.short	775
	.short	33403
	.short	839
	.short	33404
	.short	6
	.short	70
	.short	33405
	.short	134
	.short	33406
	.short	198
	.short	33407
	.short	262
	.short	326
	.short	33408
	.short	518
	.short	33409
	.short	582
	.short	33410
	.short	646
	.short	710
	.short	33411
	.short	774
	.short	33412
	.short	838
	.short	5
	.short	33413
	.short	69
	.short	33414
	.short	133
	.short	33415
	.short	197
	.short	261
	.short	33416
	.short	325
	.short	33417
	.short	517
	.short	581
	.short	33418
	.short	645
	.short	33419
	.short	709
	.short	33420
	.short	773
	.short	837
	.short	33421
	.short	4
	.short	33422
	.short	68
	.short	132
	.short	33423
	.short	196
	.short	33424
	.short	260
	.short	33425
	.short	324
	.short	516
	.short	33426
	.short	580
	.short	33427
	.short	644
	.short	708
	.short	33428
	.short	772
	.short	33429
	.short	836
	.short	33430
	.short	3
	.short	67
	.short	33431
	.short	131
	.short	33432
	.short	195
	.short	259
	.short	33433
	.short	323
	.short	33434
	.short	515
	.short	33435
	.short	579
	.short	643
	.short	33436
	.short	707
	.short	33437
	.short	771
	.short	835
	.short	33438
	.short	2
	.short	33439
	.short	66
	.short	33440
	.short	130
	.short	194
	.short	33441
	.short	258
	.short	33442
	.short	322
	.short	33443
	.short	514
	.short	578
	.short	33444
	.short	642
	.short	33445
	.short	706
	.short	770
	.short	33446
	.short	834
	.short	33447
	.short	1
	.short	33448
	.short	65
	.short	129
	.short	33449
	.short	193
	.short	33450
	.short	257
	.short	321
	.short	33451
	.short	513
	.short	33452
	.short	577
	.short	33453
	.short	641
	.short	705
	.short	33454
	.short	769
	.short	33455
	.short	833
	.short	0
	.short	33456
	.short	64
	.short	33457
	.short	128
	.short	33458
	.short	192
	.short	256
	.short	33459
	.short	320
	.short	33460
	.short	512
	.short	576
	.short	33461
	.short	640
	.short	33462
	.short	704
	.short	33463
	.short	768
	.short	832
	.short	33464
	.short	16384
	.short	33465
	.short	16640
	.short	16896
	.short	33466
	.short	17152
	.short	33467
	.short	17408
	.short	33468
	.short	18432
	.short	18688
	.short	33469
	.short	18944
	.short	33470
	.short	19200
	.short	33471
	.short	19456
	.short	16400
	.short	33472
	.short	16656
	.short	33473
	.short	16912
	.short	17168
	.short	33474
	.short	17424
	.short	33475
	.short	18448
	.short	33476
	.short	18704
	.short	18960
	.short	33477
	.short	19216
	.short	33478
	.short	19472
	.short	16416
	.short	33479
	.short	16672
	.short	33480
	.short	16928
	.short	33481
	.short	17184
	.short	17440
	.short	33482
	.short	18464
	.short	33483
	.short	18720
	.short	18976
	.short	33484
	.short	19232
	.short	33485
	.short	19488
	.short	33486
	.short	16432
	.short	16688
	.short	33487
	.short	16944
	.short	33488
	.short	17200
	.short	17456
	.short	33489
	.short	18480
	.short	33490
	.short	18736
	.short	33491
	.short	18992
	.short	19248
	.short	33492
	.short	19504
	.short	33493
	.short	16448
	.short	16704
	.short	33494
	.short	16960
	.short	33495
	.short	17216
	.short	33496
	.short	17472
	.short	18496
	.short	33497
	.short	18752
	.short	33498
	.short	19008
	.short	33499
	.short	19264
	.short	19520
	.short	33500
	.short	16464
	.short	33501
	.short	16720
	.short	16976
	.short	33502
	.short	17232
	.short	33503
	.short	17488
	.short	33504
	.short	18512
	.short	18768
	.short	33505
	.short	19024
	.short	33506
	.short	19280
	.short	19536
	.short	33507
	.short	16480
	.short	33508
	.short	16736
	.short	33509
	.short	16992
	.short	17248
	.short	33510
	.short	17504
	.short	33511
	.short	18528
	.short	18784
	.short	33512
	.short	19040
	.short	33513
	.short	19296
	.short	33514
	.short	19552
	.short	16496
	.short	33515
	.short	16752
	.short	33516
	.short	17008
	.short	17264
	.short	33517
	.short	17520
	.short	33518
	.short	18544
	.short	33519
	.short	18800
	.short	19056
	.short	33520
	.short	19312
	.short	33521
	.short	19568
	.short	16512
	.short	33522
	.short	16768
	.short	33523
	.short	17024
	.short	33524
	.short	17280
	.short	17536
	.short	33525
	.short	18560
	.short	33526
	.short	18816
	.short	33527
	.short	19072
	.short	19328
	.short	33528
	.short	19584
	.short	33529
	.short	16528
	.short	16784
	.short	33530
	.short	17040
	.short	33531
	.short	17296
	.short	33532
	.short	17552
	.short	18576
	.short	33533
	.short	18832
	.short	33534
	.short	19088
	.short	19344
	.short	33535
	.short	19600
	.short	33536
	.short	16544
	.short	33537
	.short	16800
	.short	17056
	.short	33538
	.short	17312
	.short	33539
	.short	17568
	.short	18592
	.short	33540
	.short	18848
	.short	33541
	.short	19104
	.short	33542
	.short	19360
	.short	19616
	.short	33543
	.short	16560
	.short	33544
	.short	16816
	.short	17072
	.short	33545
	.short	17328
	.short	33546
	.short	17584
	.short	33547
	.short	18608
	.short	18864
	.short	33548
	.short	19120
	.short	33549
	.short	19376
	.short	19632
	.short	33550
	.short	16576
	.short	33551
	.short	16832
	.short	33552
	.short	17088
	.short	17344
	.short	33553
	.short	17600
	.short	33554
	.short	18624
	.short	33555
	.short	18880
	.short	19136
	.short	33556
	.short	19392
	.short	33557
	.short	19648
	.short	16592
	.short	33558
	.short	16848
	.short	33559
	.short	17104
	.short	33560
	.short	17360
	.short	17616
	.short	33561
	.short	18640
	.short	33562
	.short	18896
	.short	19152
	.short	33563
	.short	19408
	.short	33564
	.short	19664
	.short	33565
	.short	16608
	.short	16864
	.short	33566
	.short	17120
	.short	33567
	.short	17376
	.short	17632
	.short	33568
	.short	18656
	.short	33569
	.short	18912
	.short	33570
	.short	19168
	.short	19424
	.short	33571
	.short	19680
	.short	33572
	.short	16385
	.short	16641
	.short	33573
	.short	16897
	.short	33574
	.short	17153
	.short	33575
	.short	17409
	.short	18433
	.short	33576
	.short	18689
	.short	33577
	.short	18945
	.short	19201
	.short	33578
	.short	19457
	.short	33579
	.short	16401
	.short	33580
	.short	16657
	.short	16913
	.short	33581
	.short	17169
	.short	33582
	.short	17425
	.short	33583
	.short	18449
	.short	18705
	.short	33584
	.short	18961
	.short	33585
	.short	19217
	.short	19473
	.short	33586
	.short	16417
	.short	33587
	.short	16673
	.short	33588
	.short	16929
	.short	17185
	.short	33589
	.short	17441
	.short	33590
	.short	18465
	.short	18721
	.short	33591
	.short	18977
	.short	33592
	.short	19233
	.short	33593
	.short	19489
	.short	16433
	.short	33594
	.short	16689
	.short	33595
	.short	16945
	.short	17201
	.short	33596
	.short	17457
	.short	33597
	.short	18481
	.short	33598
	.short	18737
	.short	18993
	.short	33599
	.short	19249
	.short	33600
	.short	19505
	.short	16449
	.short	33601
	.short	16705
	.short	33602
	.short	16961
	.short	33603
	.short	17217
	.short	17473
	.short	33604
	.short	18497
	.short	33605
	.short	18753
	.short	19009
	.short	33606
	.short	19265
	.short	33607
	.short	19521
	.short	33608
	.short	16465
	.short	16721
	.short	33609
	.short	16977
	.short	33610
	.short	17233
	.short	33611
	.short	17489
	.short	18513
	.short	33612
	.short	18769
	.short	33613
	.short	19025
	.short	19281
	.short	33614
	.short	19537
	.short	33615
	.short	16481
	.short	33616
	.short	16737
	.short	16993
	.short	33617
	.short	17249
	.short	33618
	.short	17505
	.short	18529
	.short	33619
	.short	18785
	.short	33620
	.short	19041
	.short	33621
	.short	19297
	.short	19553
	.short	33622
	.short	16497
	.short	33623
	.short	16753
	.short	17009
	.short	33624
	.short	17265
	.short	33625
	.short	17521
	.short	33626
	.short	18545
	.short	18801
	.short	33627
	.short	19057
	.short	33628
	.short	19313
	.short	19569
	.short	33629
	.short	16513
	.short	33630
	.short	16769
	.short	33631
	.short	17025
	.short	17281
	.short	33632
	.short	17537
	.short	33633
	.short	18561
	.short	18817
	.short	33634
	.short	19073
	.short	33635
	.short	19329
	.short	33636
	.short	19585
	.short	16529
	.short	33637
	.short	16785
	.short	33638
	.short	17041
	.short	33639
	.short	17297
	.short	17553
	.short	33640
	.short	18577
	.short	33641
	.short	18833
	.short	19089
	.short	33642
	.short	19345
	.short	33643
	.short	19601
	.short	33644
	.short	16545
	.short	16801
	.short	33645
	.short	17057
	.short	33646
	.short	17313
	.short	17569
	.short	33647
	.short	18593
	.short	33648
	.short	18849
	.short	33649
	.short	19105
	.short	19361
	.short	33650
	.short	19617
	.short	33651
	.short	16386
	.short	16642
	.short	33652
	.short	16898
	.short	33653
	.short	17154
	.short	33654
	.short	17410
	.short	18434
	.short	33655
	.short	18690
	.short	33656
	.short	18946
	.short	19202
	.short	33657
	.short	19458
	.short	33658
	.short	16402
	.short	33659
	.short	16658
	.short	16914
	.short	33660
	.short	17170
	.short	33661
	.short	17426
	.short	18450
	.short	33662
	.short	18706
	.short	33663
	.short	18962
	.short	33664
	.short	19218
	.short	19474
	.short	33665
	.short	16418
	.short	33666
	.short	16674
	.short	33667
	.short	16930
	.short	17186
	.short	33668
	.short	17442
	.short	33669
	.short	18466
	.short	18722
	.short	33670
	.short	18978
	.short	33671
	.short	19234
	.short	33672
	.short	19490
	.short	16434
	.short	33673
	.short	16690
	.short	33674
	.short	16946
	.short	17202
	.short	33675
	.short	17458
	.short	33676
	.short	18482
	.short	33677
	.short	18738
	.short	18994
	.short	33678
	.short	19250
	.short	33679
	.short	19506
	.short	16450
	.short	33680
	.short	16706
	.short	33681
	.short	16962
	.short	33682
	.short	17218
	.short	17474
	.short	33683
	.short	18498
	.short	33684
	.short	18754
	.short	19010
	.short	33685
	.short	19266
	.short	33686
	.short	19522
	.short	33687
	.short	16466
	.short	16722
	.short	33688
	.short	16978
	.short	33689
	.short	17234
	.short	17490
	.short	33690
	.short	18514
	.short	33691
	.short	18770
	.short	33692
	.short	19026
	.short	19282
	.short	33693
	.short	19538
	.short	33694
	.short	16482
	.short	16738
	.short	33695
	.short	16994
	.short	33696
	.short	17250
	.short	33697
	.short	17506
	.short	18530
	.short	33698
	.short	18786
	.short	33699
	.short	19042
	.short	33700
	.short	19298
	.short	19554
	.short	33701
	.short	16498
	.short	33702
	.short	16754
	.short	17010
	.short	33703
	.short	17266
	.short	33704
	.short	17522
	.short	33705
	.short	18546
	.short	18802
	.short	33706
	.short	19058
	.short	33707
	.short	19314
	.short	19570
	.short	33708
	.short	16387
	.short	33709
	.short	16643
	.short	33710
	.short	16899
	.short	17155
	.short	33711
	.short	17411
	.short	33712
	.short	18435
	.short	18691
	.short	33713
	.short	18947
	.short	33714
	.short	19203
	.short	33715
	.short	19459
	.short	16403
	.short	33716
	.short	16659
	.short	33717
	.short	16915
	.short	17171
	.short	33718
	.short	17427
	.short	33719
	.short	18451
	.short	33720
	.short	18707
	.short	18963
	.short	33721
	.short	19219
	.short	33722
	.short	19475
	.short	16419
	.short	33723
	.short	16675
	.short	33724
	.short	16931
	.short	33725
	.short	17187
	.short	17443
	.short	33726
	.short	18467
	.short	33727
	.short	18723
	.short	33728
	.short	18979
	.short	19235
	.short	33729
	.short	19491
	.short	33730
	.short	16435
	.short	16691
	.short	33731
	.short	16947
	.short	33732
	.short	17203
	.short	33733
	.short	17459
	.short	18483
	.short	33734
	.short	18739
	.short	33735
	.short	18995
	.short	19251
	.short	33736
	.short	19507
	.short	33737
	.short	16451
	.short	33738
	.short	16707
	.short	16963
	.short	33739
	.short	17219
	.short	33740
	.short	17475
	.short	18499
	.short	33741
	.short	18755
	.short	33742
	.short	19011
	.short	33743
	.short	19267
	.short	19523
	.short	33744
	.short	16467
	.short	33745
	.short	16723
	.short	16979
	.short	33746
	.short	17235
	.short	33747
	.short	17491
	.short	33748
	.short	18515
	.short	18771
	.short	33749
	.short	19027
	.short	33750
	.short	19283
	.short	19539
	.short	33751
	.short	16388
	.short	33752
	.short	16644
	.short	33753
	.short	16900
	.short	17156
	.short	33754
	.short	17412
	.short	33755
	.short	18436
	.short	33756
	.short	18692
	.short	18948
	.short	33757
	.short	19204
	.short	33758
	.short	19460
	.short	16404
	.short	33759
	.short	16660
	.short	33760
	.short	16916
	.short	33761
	.short	17172
	.short	17428
	.short	33762
	.short	18452
	.short	33763
	.short	18708
	.short	18964
	.short	33764
	.short	19220
	.short	33765
	.short	19476
	.short	33766
	.short	16420
	.short	16676
	.short	33767
	.short	16932
	.short	33768
	.short	17188
	.short	17444
	.short	33769
	.short	18468
	.short	33770
	.short	18724
	.short	33771
	.short	18980
	.short	19236
	.short	33772
	.short	19492
	.short	33773
	.short	16436
	.short	16692
	.short	33774
	.short	16948
	.short	33775
	.short	17204
	.short	33776
	.short	17460
	.short	18484
	.short	33777
	.short	18740
	.short	33778
	.short	18996
	.short	19252
	.short	33779
	.short	19508
	.short	33780
	.short	16389
	.short	33781
	.short	16645
	.short	16901
	.short	33782
	.short	17157
	.short	33783
	.short	17413
	.short	33784
	.short	18437
	.short	18693
	.short	33785
	.short	18949
	.short	33786
	.short	19205
	.short	19461
	.short	33787
	.short	16405
	.short	33788
	.short	16661
	.short	33789
	.short	16917
	.short	17173
	.short	33790
	.short	17429
	.short	33791
	.short	18453
	.short	18709
	.short	33792
	.short	18965
	.short	33793
	.short	19221
	.short	33794
	.short	19477
	.short	16421
	.short	33795
	.short	16677
	.short	33796
	.short	16933
	.short	17189
	.short	33797
	.short	17445
	.short	33798
	.short	18469
	.short	33799
	.short	18725
	.short	18981
	.short	33800
	.short	19237
	.short	33801
	.short	19493
	.short	16390
	.short	33802
	.short	16646
	.short	33803
	.short	16902
	.short	33804
	.short	17158
	.short	17414
	.short	33805
	.short	18438
	.short	33806
	.short	18694
	.short	18950
	.short	33807
	.short	19206
	.short	33808
	.short	19462
	.short	33809
	.short	16406
	.short	16662
	.short	33810
	.short	16918
	.short	33811
	.short	17174
	.short	33812
	.short	17430
	.short	18454
	.short	33813
	.short	18710
	.short	33814
	.short	18966
	.short	19222
	.short	33815
	.short	19478
	.short	33816
	.short	16391
	.short	33817
	.short	16647
	.short	16903
	.short	33818
	.short	17159
	.short	33819
	.short	17415
	.short	18439
	.short	33820
	.short	18695
	.short	33821
	.short	18951
	.short	33822
	.short	19207
	.short	19463
	.short	33823
	.short	16561
	.short	16817
	.short	17073
	.short	17329
	.short	17585
	.short	18609
	.short	18865
	.short	19121
	.short	19377
	.short	19633
	.short	16577
	.short	16833
	.short	17089
	.short	17345
	.short	17601
	.short	18625
	.short	18881
	.short	19137
	.short	19393
	.short	19649
	.short	16593
	.short	16849
	.short	17105
	.short	17361
	.short	17617
	.short	18641
	.short	18897
	.short	19153
	.short	19409
	.short	19665
	.short	16514
	.short	16770
	.short	17026
	.short	17282
	.short	17538
	.short	18562
	.short	18818
	.short	19074
	.short	19330
	.short	19586
	.short	16530
	.short	16786
	.short	17042
	.short	17298
	.short	17554
	.short	18578
	.short	18834
	.short	19090
	.short	19346
	.short	19602
	.short	16546
	.short	16802
	.short	17058
	.short	17314
	.short	17570
	.short	18594
	.short	18850
	.short	19106
	.short	19362
	.short	19618
	.short	16562
	.short	16818
	.short	17074
	.short	17330
	.short	17586
	.short	18610
	.short	18866
	.short	19122
	.short	19378
	.short	19634
	.short	16578
	.short	16834
	.short	17090
	.short	17346
	.short	17602
	.short	18626
	.short	18882
	.short	19138
	.short	19394
	.short	19650
	.short	16483
	.short	16739
	.short	16995
	.short	17251
	.short	17507
	.short	18531
	.short	18787
	.short	19043
	.short	19299
	.short	19555
	.short	16499
	.short	16755
	.short	17011
	.short	17267
	.short	17523
	.short	18547
	.short	18803
	.short	19059
	.short	19315
	.short	19571
	.short	16515
	.short	16771
	.short	17027
	.short	17283
	.short	17539
	.short	18563
	.short	18819
	.short	19075
	.short	19331
	.short	19587
	.short	16531
	.short	16787
	.short	17043
	.short	17299
	.short	17555
	.short	18579
	.short	18835
	.short	19091
	.short	19347
	.short	19603
	.short	16547
	.short	16803
	.short	17059
	.short	17315
	.short	17571
	.short	18595
	.short	18851
	.short	19107
	.short	19363
	.short	19619
	.short	16563
	.short	16819
	.short	17075
	.short	17331
	.short	17587
	.short	18611
	.short	18867
	.short	19123
	.short	19379
	.short	19635
	.short	16452
	.short	16708
	.short	16964
	.short	17220
	.short	17476
	.short	18500
	.short	18756
	.short	19012
	.short	19268
	.short	19524
	.short	16468
	.short	16724
	.short	16980
	.short	17236
	.short	17492
	.short	18516
	.short	18772
	.short	19028
	.short	19284
	.short	19540
	.short	16484
	.short	16740
	.short	16996
	.short	17252
	.short	17508
	.short	18532
	.short	18788
	.short	19044
	.short	19300
	.short	19556
	.short	16500
	.short	16756
	.short	17012
	.short	17268
	.short	17524
	.short	18548
	.short	18804
	.short	19060
	.short	19316
	.short	19572
	.short	16516
	.short	16772
	.short	17028
	.short	17284
	.short	17540
	.short	18564
	.short	18820
	.short	19076
	.short	19332
	.short	19588
	.short	16532
	.short	16788
	.short	17044
	.short	17300
	.short	17556
	.short	18580
	.short	18836
	.short	19092
	.short	19348
	.short	19604
	.short	16548
	.short	16804
	.short	17060
	.short	17316
	.short	17572
	.short	18596
	.short	18852
	.short	19108
	.short	19364
	.short	19620
	.short	16437
	.short	16693
	.short	16949
	.short	17205
	.short	17461
	.short	18485
	.short	18741
	.short	18997
	.short	19253
	.short	19509
	.short	16453
	.short	16709
	.short	16965
	.short	17221
	.short	17477
	.short	18501
	.short	18757
	.short	19013
	.short	19269
	.short	19525
	.short	16469
	.short	16725
	.short	16981
	.short	17237
	.short	17493
	.short	18517
	.short	18773
	.short	19029
	.short	19285
	.short	19541
	.short	16485
	.short	16741
	.short	16997
	.short	17253
	.short	17509
	.short	18533
	.short	18789
	.short	19045
	.short	19301
	.short	19557
	.short	16501
	.short	16757
	.short	17013
	.short	17269
	.short	17525
	.short	18549
	.short	18805
	.short	19061
	.short	19317
	.short	19573
	.short	16517
	.short	16773
	.short	17029
	.short	17285
	.short	17541
	.short	18565
	.short	18821
	.short	19077
	.short	19333
	.short	19589
	.short	16533
	.short	16789
	.short	17045
	.short	17301
	.short	17557
	.short	18581
	.short	18837
	.short	19093
	.short	19349
	.short	19605
	.short	16422
	.short	16678
	.short	16934
	.short	17190
	.short	17446
	.short	18470
	.short	18726
	.short	18982
	.short	19238
	.short	19494
	.short	16438
	.short	16694
	.short	16950
	.short	17206
	.short	17462
	.short	18486
	.short	18742
	.short	18998
	.short	19254
	.short	19510
	.short	16454
	.short	16710
	.short	16966
	.short	17222
	.short	17478
	.short	18502
	.short	18758
	.short	19014
	.short	19270
	.short	19526
	.short	16470
	.short	16726
	.short	16982
	.short	17238
	.short	17494
	.short	18518
	.short	18774
	.short	19030
	.short	19286
	.short	19542
	.short	16486
	.short	16742
	.short	16998
	.short	17254
	.short	17510
	.short	18534
	.short	18790
	.short	19046
	.short	19302
	.short	19558
	.short	16502
	.short	16758
	.short	17014
	.short	17270
	.short	17526
	.short	18550
	.short	18806
	.short	19062
	.short	19318
	.short	19574
	.short	16518
	.short	16774
	.short	17030
	.short	17286
	.short	17542
	.short	18566
	.short	18822
	.short	19078
	.short	19334
	.short	19590
	.short	16407
	.short	16663
	.short	16919
	.short	17175
	.short	17431
	.short	18455
	.short	18711
	.short	18967
	.short	19223
	.short	19479
	.short	16423
	.short	16679
	.short	16935
	.short	17191
	.short	17447
	.short	18471
	.short	18727
	.short	18983
	.short	19239
	.short	19495
	.short	16439
	.short	16695
	.short	16951
	.short	17207
	.short	17463
	.short	18487
	.short	18743
	.short	18999
	.short	19255
	.short	19511
	.short	16455
	.short	16711
	.short	16967
	.short	17223
	.short	17479
	.short	18503
	.short	18759
	.short	19015
	.short	19271
	.short	19527
	.short	16471
	.short	16727
	.short	16983
	.short	17239
	.short	17495
	.short	18519
	.short	18775
	.short	19031
	.short	19287
	.short	19543
	.short	16487
	.short	16743
	.short	16999
	.short	17255
	.short	17511
	.short	18535
	.short	18791
	.short	19047
	.short	19303
	.short	19559
	.short	16503
	.short	16759
	.short	17015
	.short	17271
	.short	17527
	.short	18551
	.short	18807
	.short	19063
	.short	19319
	.short	19575
	.short	16392
	.short	16648
	.short	16904
	.short	17160
	.short	17416
	.short	18440
	.short	18696
	.short	18952
	.short	19208
	.short	19464
	.short	16408
	.short	16664
	.short	16920
	.short	17176
	.short	17432
	.short	18456
	.short	18712
	.short	18968
	.short	19224
	.short	19480
	.short	16424
	.short	16680
	.short	16936
	.short	17192
	.short	17448
	.short	18472
	.short	18728
	.short	18984
	.short	19240
	.short	19496
	.short	16440
	.short	16696
	.short	16952
	.short	17208
	.short	17464
	.short	18488
	.short	18744
	.short	19000
	.short	19256
	.short	19512
	.short	16456
	.short	16712
	.short	16968
	.short	17224
	.short	17480
	.short	18504
	.short	18760
	.short	19016
	.short	19272
	.short	19528
	.short	16472
	.short	16728
	.short	16984
	.short	17240
	.short	17496
	.short	18520
	.short	18776
	.short	19032
	.short	19288
	.short	19544
	.short	16488
	.short	16744
	.short	17000
	.short	17256
	.short	17512
	.short	18536
	.short	18792
	.short	19048
	.short	19304
	.short	19560
	.short	16393
	.short	16649
	.short	16905
	.short	17161
	.short	17417
	.short	18441
	.short	18697
	.short	18953
	.short	19209
	.short	19465
	.short	16409
	.short	16665
	.short	16921
	.short	17177
	.short	17433
	.short	18457
	.short	18713
	.short	18969
	.short	19225
	.short	19481
	.short	16425
	.short	16681
	.short	16937
	.short	17193
	.short	17449
	.short	18473
	.short	18729
	.short	18985
	.short	19241
	.short	19497
	.short	16441
	.short	16697
	.short	16953
	.short	17209
	.short	17465
	.short	18489
	.short	18745
	.short	19001
	.short	19257
	.short	19513
	.short	16457
	.short	16713
	.short	16969
	.short	17225
	.short	17481
	.short	18505
	.short	18761
	.short	19017
	.short	19273
	.short	19529
	.short	16473
	.short	16729
	.short	16985
	.short	17241
	.short	17497
	.short	18521
	.short	18777
	.short	19033
	.short	19289
	.short	19545
	.short	16394
	.short	16650
	.short	16906
	.short	17162
	.short	17418
	.short	18442
	.short	18698
	.short	18954
	.short	19210
	.short	19466
	.short	16410
	.short	16666
	.short	16922
	.short	17178
	.short	17434
	.short	18458
	.short	18714
	.short	18970
	.short	19226
	.short	19482
	.short	16426
	.short	16682
	.short	16938
	.short	17194
	.short	17450
	.short	18474
	.short	18730
	.short	18986
	.short	19242
	.short	19498
	.short	16442
	.short	16698
	.short	16954
	.short	17210
	.short	17466
	.short	18490
	.short	18746
	.short	19002
	.short	19258
	.short	19514
	.short	16458
	.short	16714
	.short	16970
	.short	17226
	.short	17482
	.short	18506
	.short	18762
	.short	19018
	.short	19274
	.short	19530
	.short	16395
	.short	16651
	.short	16907
	.short	17163
	.short	17419
	.short	18443
	.short	18699
	.short	18955
	.short	19211
	.short	19467
	.short	16411
	.short	16667
	.short	16923
	.short	17179
	.short	17435
	.short	18459
	.short	18715
	.short	18971
	.short	19227
	.short	19483
	.short	16427
	.short	16683
	.short	16939
	.short	17195
	.short	17451
	.short	18475
	.short	18731
	.short	18987
	.short	19243
	.short	19499
	.short	16443
	.short	16699
	.short	16955
	.short	17211
	.short	17467
	.short	18491
	.short	18747
	.short	19003
	.short	19259
	.short	19515
	.short	16396
	.short	16652
	.short	16908
	.short	17164
	.short	17420
	.short	18444
	.short	18700
	.short	18956
	.short	19212
	.short	19468
	.short	16412
	.short	16668
	.short	16924
	.short	17180
	.short	17436
	.short	18460
	.short	18716
	.short	18972
	.short	19228
	.short	19484
	.short	16428
	.short	16684
	.short	16940
	.short	17196
	.short	17452
	.short	18476
	.short	18732
	.short	18988
	.short	19244
	.short	19500
	.short	16397
	.short	16653
	.short	16909
	.short	17165
	.short	17421
	.short	18445
	.short	18701
	.short	18957
	.short	19213
	.short	19469
	.short	16413
	.short	16669
	.short	16925
	.short	17181
	.short	17437
	.short	18461
	.short	18717
	.short	18973
	.short	19229
	.short	19485
	.short	16398
	.short	16654
	.short	16910
	.short	17166
	.short	17422
	.short	18446
	.short	18702
	.short	18958
	.short	19214
	.short	19470
	.size	_ZN3attL9ATT_ORDERE, 6604

	.type	__hip_cuid_5ba2c1623d679635,@object
